# v57 + wave_sum butterflies in P0 (XB/SS rows) and final rmsnorm: ds_bpermute xor steps replaced by DPP movs (quad_perm, row_half_mirror, row_mirror) and v_permlane16/32_swap, same additions (bit-ident
# baseline (speedup 1.0000x reference)
; __device__ __forceinline__ unsigned pk2(float lo, float hi) { return pg8::cvt_pk_bf16(lo, hi); }
; __device__ __forceinline__ float wave_sum(float v) {
; #pragma unroll
;     for (int o = 1; o < 64; o <<= 1) v += __shfl_xor(v, o);
;     return v;
; }
; __global__ void __launch_bounds__(NTHR, 2) hybrid_fwd(Args args) {
;     ...
;         for (int m0 = gw; m0 < M; m0 += 4 * NGW) {
;             f32x4 xv[4][4];
; #pragma unroll
;             for (int r = 0; r < 4; ++r) { const int m = (m0 + r * NGW < M) ? m0 + r * NGW : m0; const f32x4* xr = (const f32x4*)(args.x + (size_t)m * D) + lane;
; #pragma unroll
;                 for (int j = 0; j < 4; ++j) xv[r][j] = __builtin_nontemporal_load(xr + 64 * j); }
; #pragma unroll
;             for (int r = 0; r < 4; ++r) { const int m = m0 + r * NGW; if (m >= M) continue; float s = 0.f;
;                 unsigned long long* o8 = (unsigned long long*)(XB + (size_t)m * D) + lane;
; #pragma unroll
;                 for (int j = 0; j < 4; ++j) { const f32x4 v = xv[r][j]; s += (v[0] * v[0] + v[1] * v[1]) + (v[2] * v[2] + v[3] * v[3]);
;                     o8[64 * j] = (unsigned long long)pk2(v[0], v[1]) | ((unsigned long long)pk2(v[2], v[3]) << 32); }
;                 s = wave_sum(s);
;                 if (lane < 16) SS[(size_t)m * 16 + lane] = (lane == 0) ? s : 0.f; }
.LBB0_155:
	s_ashr_i32 s7, s6, 31
	s_add_i32 s18, s33, s6
	s_cmpk_lt_i32 s18, 0x4000
	s_cselect_b32 s24, s18, s6
	s_ashr_i32 s25, s24, 31
	s_lshl_b64 s[24:25], s[24:25], 12
	s_add_i32 s38, s82, s6
	s_cmpk_lt_i32 s38, 0x4000
	v_lshl_add_u64 v[130:131], v[186:187], 0, s[24:25]
	s_cselect_b32 s24, s38, s6
	s_ashr_i32 s25, s24, 31
	s_lshl_b64 s[24:25], s[24:25], 12
	s_add_i32 s36, s93, s6
	s_cmpk_lt_i32 s36, 0x4000
	global_load_dwordx4 v[174:177], v[130:131], off nt
	global_load_dwordx4 v[170:173], v[130:131], off offset:1024 nt
	s_waitcnt lgkmcnt(0)
	global_load_dwordx4 v[166:169], v[130:131], off offset:2048 nt
	global_load_dwordx4 v[162:165], v[130:131], off offset:3072 nt
	v_lshl_add_u64 v[130:131], v[186:187], 0, s[24:25]
	s_cselect_b32 s24, s36, s6
	s_ashr_i32 s25, s24, 31
	s_lshl_b64 s[24:25], s[24:25], 12
	global_load_dwordx4 v[158:161], v[130:131], off nt
	global_load_dwordx4 v[154:157], v[130:131], off offset:1024 nt
	global_load_dwordx4 v[150:153], v[130:131], off offset:2048 nt
	global_load_dwordx4 v[146:149], v[130:131], off offset:3072 nt
	v_lshl_add_u64 v[130:131], v[186:187], 0, s[24:25]
	s_lshl_b64 s[24:25], s[6:7], 12
	v_lshl_add_u64 v[192:193], v[186:187], 0, s[24:25]
	global_load_dwordx4 v[142:145], v[130:131], off nt
	global_load_dwordx4 v[138:141], v[130:131], off offset:1024 nt
	global_load_dwordx4 v[134:137], v[130:131], off offset:2048 nt
	s_nop 0
	global_load_dwordx4 v[130:133], v[130:131], off offset:3072 nt
	s_nop 0
	global_load_dwordx4 v[178:181], v[192:193], off offset:3072 nt
	global_load_dwordx4 v[200:203], v[192:193], off offset:2048 nt
	global_load_dwordx4 v[204:207], v[192:193], off offset:1024 nt
	global_load_dwordx4 v[208:211], v[192:193], off nt
	s_lshl_b64 s[24:25], s[6:7], 11
	v_lshl_add_u64 v[192:193], v[188:189], 0, s[24:25]
	s_waitcnt vmcnt(0)
	v_mul_f32_e32 v212, v209, v209
	v_fmac_f32_e32 v212, v208, v208
	v_cvt_pk_bf16_f32 v208, v208, v209
	v_cvt_pk_bf16_f32 v209, v210, v211
	global_store_dwordx2 v[192:193], v[208:209], off
	v_mul_f32_e32 v208, v205, v205
	v_fmac_f32_e32 v208, v204, v204
	v_cvt_pk_bf16_f32 v204, v204, v205
	v_cvt_pk_bf16_f32 v205, v206, v207
	v_mul_f32_e32 v213, v211, v211
	v_mul_f32_e32 v209, v207, v207
	global_store_dwordx2 v[192:193], v[204:205], off offset:512
	v_mul_f32_e32 v204, v201, v201
	v_fmac_f32_e32 v213, v210, v210
	v_fmac_f32_e32 v209, v206, v206
	v_fmac_f32_e32 v204, v200, v200
	v_mul_f32_e32 v205, v203, v203
	v_cvt_pk_bf16_f32 v200, v200, v201
	v_cvt_pk_bf16_f32 v201, v202, v203
	v_add_f32_e32 v212, v212, v213
	v_add_f32_e32 v208, v208, v209
	v_fmac_f32_e32 v205, v202, v202
	global_store_dwordx2 v[192:193], v[200:201], off offset:1024
	v_mul_f32_e32 v200, v179, v179
	v_mul_f32_e32 v201, v181, v181
	v_add_f32_e32 v208, v212, v208
	v_add_f32_e32 v204, v204, v205
	v_fmac_f32_e32 v200, v178, v178
	v_fmac_f32_e32 v201, v180, v180
	v_add_f32_e32 v204, v208, v204
	v_add_f32_e32 v200, v200, v201
	v_add_f32_e32 v200, v204, v200
	v_cvt_pk_bf16_f32 v178, v178, v179
	v_cvt_pk_bf16_f32 v179, v180, v181
	global_store_dwordx2 v[192:193], v[178:179], off offset:1536
	s_nop 1
	v_mov_b32_dpp v178, v200 quad_perm:[1,0,3,2] row_mask:0xf bank_mask:0xf
	s_waitcnt lgkmcnt(0)
	v_add_f32_e32 v178, v200, v178
	s_nop 1
	v_mov_b32_dpp v179, v178 quad_perm:[2,3,0,1] row_mask:0xf bank_mask:0xf
	s_waitcnt lgkmcnt(0)
	v_add_f32_e32 v178, v178, v179
	s_nop 1
	v_mov_b32_dpp v179, v178 row_half_mirror row_mask:0xf bank_mask:0xf
	s_waitcnt lgkmcnt(0)
	v_add_f32_e32 v178, v178, v179
	s_nop 1
	v_mov_b32_dpp v179, v178 row_mirror row_mask:0xf bank_mask:0xf
	s_waitcnt lgkmcnt(0)
	v_add_f32_e32 v178, v178, v179
	v_mov_b32_e32 v179, v178
	v_mov_b32_e32 v198, v178
	s_nop 1
	v_permlane16_swap_b32 v179, v198
	s_nop 1
	s_waitcnt lgkmcnt(0)
	v_add_f32_e32 v178, v179, v198
	v_mov_b32_e32 v179, v178
	v_mov_b32_e32 v199, v178
	s_nop 1
	v_permlane32_swap_b32 v179, v199
	s_nop 1
	s_and_saveexec_b64 s[24:25], vcc
	s_cbranch_execz .LBB0_161
	s_lshl_b64 s[26:27], s[6:7], 6
	s_waitcnt lgkmcnt(0)
	v_add_f32_e32 v178, v179, v199
	v_lshl_add_u64 v[180:181], v[190:191], 0, s[26:27]
	v_cndmask_b32_e64 v178, 0, v178, s[4:5]
	global_store_dword v[180:181], v178, off
	s_or_b64 exec, exec, s[24:25]
	s_cmpk_gt_i32 s18, 0x3fff
	s_cbranch_scc0 .LBB0_162

; __device__ __forceinline__ unsigned pk2(float lo, float hi) { return pg8::cvt_pk_bf16(lo, hi); }
; __device__ __forceinline__ float wave_sum(float v) {
; #pragma unroll
;     for (int o = 1; o < 64; o <<= 1) v += __shfl_xor(v, o);
;     return v;
; }
; __global__ void __launch_bounds__(NTHR, 2) hybrid_fwd(Args args) {
;     ...
;             for (int r = 0; r < 4; ++r) { const int m = m0 + r * NGW; if (m >= M) continue; float s = 0.f;
;                 unsigned long long* o8 = (unsigned long long*)(XB + (size_t)m * D) + lane;
; #pragma unroll
;                 for (int j = 0; j < 4; ++j) { const f32x4 v = xv[r][j]; s += (v[0] * v[0] + v[1] * v[1]) + (v[2] * v[2] + v[3] * v[3]);
;                     o8[64 * j] = (unsigned long long)pk2(v[0], v[1]) | ((unsigned long long)pk2(v[2], v[3]) << 32); }
;                 s = wave_sum(s);
;                 if (lane < 16) SS[(size_t)m * 16 + lane] = (lane == 0) ? s : 0.f; }
.LBB0_158:
	v_mul_f32_e32 v162, v159, v159
	v_mul_f32_e32 v163, v161, v161
	v_fmac_f32_e32 v162, v158, v158
	v_fmac_f32_e32 v163, v160, v160
	v_add_f32_e32 v162, v162, v163
	v_mul_f32_e32 v163, v155, v155
	v_mul_f32_e32 v164, v157, v157
	v_fmac_f32_e32 v163, v154, v154
	v_fmac_f32_e32 v164, v156, v156
	v_add_f32_e32 v163, v163, v164
	v_add_f32_e32 v162, v162, v163
	v_mul_f32_e32 v163, v151, v151
	v_mul_f32_e32 v164, v153, v153
	v_fmac_f32_e32 v163, v150, v150
	v_fmac_f32_e32 v164, v152, v152
	v_add_f32_e32 v163, v163, v164
	v_add_f32_e32 v162, v162, v163
	v_mul_f32_e32 v163, v147, v147
	v_mul_f32_e32 v164, v149, v149
	v_fmac_f32_e32 v163, v146, v146
	v_fmac_f32_e32 v164, v148, v148
	v_add_f32_e32 v163, v163, v164
	v_add_f32_e32 v162, v162, v163
	s_nop 1
	v_mov_b32_dpp v163, v162 quad_perm:[1,0,3,2] row_mask:0xf bank_mask:0xf
	s_ashr_i32 s39, s38, 31
	s_lshl_b64 s[18:19], s[38:39], 11
	v_cvt_pk_bf16_f32 v158, v158, v159
	v_cvt_pk_bf16_f32 v159, v160, v161
	s_waitcnt lgkmcnt(0)
	v_add_f32_e32 v162, v162, v163
	s_nop 1
	v_mov_b32_dpp v163, v162 quad_perm:[2,3,0,1] row_mask:0xf bank_mask:0xf
	v_cvt_pk_bf16_f32 v154, v154, v155
	v_cvt_pk_bf16_f32 v155, v156, v157
	v_cvt_pk_bf16_f32 v146, v146, v147
	v_cvt_pk_bf16_f32 v147, v148, v149
	s_waitcnt lgkmcnt(0)
	v_add_f32_e32 v164, v162, v163
	s_nop 1
	v_mov_b32_dpp v165, v164 row_half_mirror row_mask:0xf bank_mask:0xf
	v_lshl_add_u64 v[162:163], v[188:189], 0, s[18:19]
	global_store_dwordx2 v[162:163], v[158:159], off
	global_store_dwordx2 v[162:163], v[154:155], off offset:512
	v_cvt_pk_bf16_f32 v154, v150, v151
	s_waitcnt lgkmcnt(0)
	v_add_f32_e32 v164, v164, v165
	s_nop 1
	v_mov_b32_dpp v165, v164 row_mirror row_mask:0xf bank_mask:0xf
	v_cvt_pk_bf16_f32 v155, v152, v153
	global_store_dwordx2 v[162:163], v[154:155], off offset:1024
	global_store_dwordx2 v[162:163], v[146:147], off offset:1536
	s_waitcnt lgkmcnt(0)
	v_add_f32_e32 v158, v164, v165
	v_mov_b32_e32 v159, v158
	v_mov_b32_e32 v198, v158
	s_nop 1
	v_permlane16_swap_b32 v159, v198
	s_nop 1
	s_waitcnt lgkmcnt(0)
	v_add_f32_e32 v150, v159, v198
	v_mov_b32_e32 v151, v150
	v_mov_b32_e32 v199, v150
	s_nop 1
	v_permlane32_swap_b32 v151, v199
	s_nop 1
	s_and_saveexec_b64 s[18:19], vcc
	s_cbranch_execz .LBB0_160
	s_lshl_b64 s[24:25], s[38:39], 6
	s_waitcnt lgkmcnt(0)
	v_add_f32_e32 v148, v151, v199
	v_lshl_add_u64 v[146:147], v[190:191], 0, s[24:25]
	v_cndmask_b32_e64 v148, 0, v148, s[4:5]
	global_store_dword v[146:147], v148, off

; __device__ __forceinline__ unsigned pk2(float lo, float hi) { return pg8::cvt_pk_bf16(lo, hi); }
; __device__ __forceinline__ float wave_sum(float v) {
; #pragma unroll
;     for (int o = 1; o < 64; o <<= 1) v += __shfl_xor(v, o);
;     return v;
; }
; __global__ void __launch_bounds__(NTHR, 2) hybrid_fwd(Args args) {
;     ...
;             for (int r = 0; r < 4; ++r) { const int m = m0 + r * NGW; if (m >= M) continue; float s = 0.f;
;                 unsigned long long* o8 = (unsigned long long*)(XB + (size_t)m * D) + lane;
; #pragma unroll
;                 for (int j = 0; j < 4; ++j) { const f32x4 v = xv[r][j]; s += (v[0] * v[0] + v[1] * v[1]) + (v[2] * v[2] + v[3] * v[3]);
;                     o8[64 * j] = (unsigned long long)pk2(v[0], v[1]) | ((unsigned long long)pk2(v[2], v[3]) << 32); }
;                 s = wave_sum(s);
;                 if (lane < 16) SS[(size_t)m * 16 + lane] = (lane == 0) ? s : 0.f; }
.LBB0_162:
	v_mul_f32_e32 v178, v175, v175
	s_waitcnt lgkmcnt(0)
	v_mul_f32_e32 v179, v177, v177
	v_fmac_f32_e32 v178, v174, v174
	v_fmac_f32_e32 v179, v176, v176
	v_add_f32_e32 v178, v178, v179
	v_mul_f32_e32 v179, v171, v171
	v_mul_f32_e32 v180, v173, v173
	v_fmac_f32_e32 v179, v170, v170
	v_fmac_f32_e32 v180, v172, v172
	v_add_f32_e32 v179, v179, v180
	v_add_f32_e32 v178, v178, v179
	v_mul_f32_e32 v179, v167, v167
	v_mul_f32_e32 v180, v169, v169
	v_fmac_f32_e32 v179, v166, v166
	v_fmac_f32_e32 v180, v168, v168
	v_add_f32_e32 v179, v179, v180
	v_add_f32_e32 v178, v178, v179
	v_mul_f32_e32 v179, v163, v163
	v_mul_f32_e32 v180, v165, v165
	v_fmac_f32_e32 v179, v162, v162
	v_fmac_f32_e32 v180, v164, v164
	v_add_f32_e32 v179, v179, v180
	v_add_f32_e32 v178, v178, v179
	s_nop 1
	v_mov_b32_dpp v179, v178 quad_perm:[1,0,3,2] row_mask:0xf bank_mask:0xf
	s_ashr_i32 s19, s18, 31
	s_lshl_b64 s[24:25], s[18:19], 11
	v_cvt_pk_bf16_f32 v174, v174, v175
	v_cvt_pk_bf16_f32 v175, v176, v177
	s_waitcnt lgkmcnt(0)
	v_add_f32_e32 v178, v178, v179
	s_nop 1
	v_mov_b32_dpp v179, v178 quad_perm:[2,3,0,1] row_mask:0xf bank_mask:0xf
	v_cvt_pk_bf16_f32 v170, v170, v171
	v_cvt_pk_bf16_f32 v171, v172, v173
	v_cvt_pk_bf16_f32 v162, v162, v163
	v_cvt_pk_bf16_f32 v163, v164, v165
	s_waitcnt lgkmcnt(0)
	v_add_f32_e32 v180, v178, v179
	s_nop 1
	v_mov_b32_dpp v181, v180 row_half_mirror row_mask:0xf bank_mask:0xf
	v_lshl_add_u64 v[178:179], v[188:189], 0, s[24:25]
	global_store_dwordx2 v[178:179], v[174:175], off
	global_store_dwordx2 v[178:179], v[170:171], off offset:512
	v_cvt_pk_bf16_f32 v170, v166, v167
	s_waitcnt lgkmcnt(0)
	v_add_f32_e32 v180, v180, v181
	s_nop 1
	v_mov_b32_dpp v181, v180 row_mirror row_mask:0xf bank_mask:0xf
	v_cvt_pk_bf16_f32 v171, v168, v169
	global_store_dwordx2 v[178:179], v[170:171], off offset:1024
	global_store_dwordx2 v[178:179], v[162:163], off offset:1536
	s_waitcnt lgkmcnt(0)
	v_add_f32_e32 v174, v180, v181
	v_mov_b32_e32 v175, v174
	v_mov_b32_e32 v198, v174
	s_nop 1
	v_permlane16_swap_b32 v175, v198
	s_nop 1
	s_waitcnt lgkmcnt(0)
	v_add_f32_e32 v166, v175, v198
	v_mov_b32_e32 v167, v166
	v_mov_b32_e32 v199, v166
	s_nop 1
	v_permlane32_swap_b32 v167, v199
	s_nop 1
	s_and_saveexec_b64 s[24:25], vcc
	s_cbranch_execz .LBB0_164
	s_lshl_b64 s[18:19], s[18:19], 6
	s_waitcnt lgkmcnt(0)
	v_add_f32_e32 v164, v167, v199
	v_lshl_add_u64 v[162:163], v[190:191], 0, s[18:19]
	v_cndmask_b32_e64 v164, 0, v164, s[4:5]
	global_store_dword v[162:163], v164, off

; __device__ __forceinline__ unsigned pk2(float lo, float hi) { return pg8::cvt_pk_bf16(lo, hi); }
; __device__ __forceinline__ float wave_sum(float v) {
; #pragma unroll
;     for (int o = 1; o < 64; o <<= 1) v += __shfl_xor(v, o);
;     return v;
; }
; __global__ void __launch_bounds__(NTHR, 2) hybrid_fwd(Args args) {
;     ...
;             for (int r = 0; r < 4; ++r) { const int m = m0 + r * NGW; if (m >= M) continue; float s = 0.f;
;                 unsigned long long* o8 = (unsigned long long*)(XB + (size_t)m * D) + lane;
; #pragma unroll
;                 for (int j = 0; j < 4; ++j) { const f32x4 v = xv[r][j]; s += (v[0] * v[0] + v[1] * v[1]) + (v[2] * v[2] + v[3] * v[3]);
;                     o8[64 * j] = (unsigned long long)pk2(v[0], v[1]) | ((unsigned long long)pk2(v[2], v[3]) << 32); }
;                 s = wave_sum(s);
;                 if (lane < 16) SS[(size_t)m * 16 + lane] = (lane == 0) ? s : 0.f; }
.LBB0_166:
	v_mul_f32_e32 v146, v143, v143
	v_mul_f32_e32 v147, v145, v145
	v_fmac_f32_e32 v146, v142, v142
	v_fmac_f32_e32 v147, v144, v144
	v_add_f32_e32 v146, v146, v147
	v_mul_f32_e32 v147, v139, v139
	v_mul_f32_e32 v148, v141, v141
	v_fmac_f32_e32 v147, v138, v138
	v_fmac_f32_e32 v148, v140, v140
	v_add_f32_e32 v147, v147, v148
	v_add_f32_e32 v146, v146, v147
	v_mul_f32_e32 v147, v135, v135
	v_mul_f32_e32 v148, v137, v137
	v_fmac_f32_e32 v147, v134, v134
	v_fmac_f32_e32 v148, v136, v136
	v_add_f32_e32 v147, v147, v148
	v_add_f32_e32 v146, v146, v147
	v_mul_f32_e32 v147, v131, v131
	v_mul_f32_e32 v148, v133, v133
	v_fmac_f32_e32 v147, v130, v130
	v_fmac_f32_e32 v148, v132, v132
	v_add_f32_e32 v147, v147, v148
	v_add_f32_e32 v146, v146, v147
	s_nop 1
	v_mov_b32_dpp v147, v146 quad_perm:[1,0,3,2] row_mask:0xf bank_mask:0xf
	s_ashr_i32 s37, s36, 31
	s_lshl_b64 s[18:19], s[36:37], 11
	v_cvt_pk_bf16_f32 v142, v142, v143
	v_cvt_pk_bf16_f32 v143, v144, v145
	s_waitcnt lgkmcnt(0)
	v_add_f32_e32 v146, v146, v147
	s_nop 1
	v_mov_b32_dpp v147, v146 quad_perm:[2,3,0,1] row_mask:0xf bank_mask:0xf
	v_cvt_pk_bf16_f32 v138, v138, v139
	v_cvt_pk_bf16_f32 v139, v140, v141
	v_cvt_pk_bf16_f32 v130, v130, v131
	v_cvt_pk_bf16_f32 v131, v132, v133
	s_waitcnt lgkmcnt(0)
	v_add_f32_e32 v148, v146, v147
	s_nop 1
	v_mov_b32_dpp v149, v148 row_half_mirror row_mask:0xf bank_mask:0xf
	v_lshl_add_u64 v[146:147], v[188:189], 0, s[18:19]
	global_store_dwordx2 v[146:147], v[142:143], off
	global_store_dwordx2 v[146:147], v[138:139], off offset:512
	v_cvt_pk_bf16_f32 v138, v134, v135
	s_waitcnt lgkmcnt(0)
	v_add_f32_e32 v148, v148, v149
	s_nop 1
	v_mov_b32_dpp v149, v148 row_mirror row_mask:0xf bank_mask:0xf
	v_cvt_pk_bf16_f32 v139, v136, v137
	global_store_dwordx2 v[146:147], v[138:139], off offset:1024
	global_store_dwordx2 v[146:147], v[130:131], off offset:1536
	s_waitcnt lgkmcnt(0)
	v_add_f32_e32 v142, v148, v149
	v_mov_b32_e32 v143, v142
	v_mov_b32_e32 v198, v142
	s_nop 1
	v_permlane16_swap_b32 v143, v198
	s_nop 1
	s_waitcnt lgkmcnt(0)
	v_add_f32_e32 v134, v143, v198
	v_mov_b32_e32 v135, v134
	v_mov_b32_e32 v199, v134
	s_nop 1
	v_permlane32_swap_b32 v135, v199
	s_nop 1
	s_and_saveexec_b64 s[18:19], vcc
	s_cbranch_execz .LBB0_153
	s_lshl_b64 s[24:25], s[36:37], 6
	s_waitcnt lgkmcnt(0)
	v_add_f32_e32 v132, v135, v199
	v_lshl_add_u64 v[130:131], v[190:191], 0, s[24:25]
	v_cndmask_b32_e64 v132, 0, v132, s[4:5]
	global_store_dword v[130:131], v132, off
	s_branch .LBB0_153

; __device__ __forceinline__ float wave_sum(float v) {
; #pragma unroll
;     for (int o = 1; o < 64; o <<= 1) v += __shfl_xor(v, o);
;     return v;
; }
; template <int layer> __device__ __forceinline__ void layer_phases(const Ctx& c, unsigned char* lds) {
;     ...
; #pragma unroll
;                         for (int j = 0; j < 4; ++j) s += (v[j][0] * v[j][0] + v[j][1] * v[j][1]) + (v[j][2] * v[j][2] + v[j][3] * v[j][3]);
;                         const float rs = __builtin_amdgcn_rsqf(wave_sum(s) * (1.0f / D) + pg8::RMS_EPS);
;                         f32x4* xr = (f32x4*)(X + (size_t)m * D) + lane;
; #pragma unroll
;                         for (int j = 0; j < 4; ++j) __builtin_nontemporal_store(v[j] * rs * gfv[j], xr + 64 * j); }
.LBB0_1908:
	v_pk_mul_f32 v[16:17], v[34:35], v[34:35]
	v_pk_mul_f32 v[18:19], v[32:33], v[32:33]
	s_ashr_i32 s11, s10, 31
	v_pk_mov_b32 v[20:21], v[18:19], v[16:17] op_sel:[1,0]
	v_mov_b32_e32 v19, v17
	v_pk_add_f32 v[16:17], v[20:21], v[18:19]
	v_pk_mul_f32 v[18:19], v[38:39], v[38:39]
	v_pk_add_f32 v[16:17], v[16:17], v[16:17] op_sel_hi:[0,1]
	v_pk_mul_f32 v[20:21], v[36:37], v[36:37]
	v_mul_f32_e32 v16, v40, v40
	v_pk_mov_b32 v[22:23], v[20:21], v[18:19] op_sel:[1,0]
	v_mov_b32_e32 v21, v19
	v_pk_add_f32 v[18:19], v[22:23], v[20:21]
	v_pk_fma_f32 v[20:21], v[40:41], v[40:41], v[16:17] op_sel_hi:[1,1,0]
	v_mul_f32_e32 v16, v42, v42
	v_pk_add_f32 v[18:19], v[18:19], v[18:19] op_sel_hi:[0,1]
	v_pk_fma_f32 v[22:23], v[42:43], v[42:43], v[16:17] op_sel_hi:[1,1,0]
	v_mul_f32_e32 v20, v44, v44
	v_mul_f32_e32 v22, v45, v45
	v_mul_f32_e32 v18, v46, v46
	v_mul_f32_e32 v16, v47, v47
	v_pk_add_f32 v[20:21], v[20:21], v[22:23]
	v_pk_add_f32 v[16:17], v[18:19], v[16:17]
	s_lshl_b64 s[10:11], s[10:11], 12
	v_pk_add_f32 v[16:17], v[20:21], v[16:17]
	v_lshl_add_u64 v[26:27], v[54:55], 0, s[10:11]
	v_add_f32_e32 v16, v16, v17
	s_nop 1
	v_mov_b32_dpp v17, v16 quad_perm:[1,0,3,2] row_mask:0xf bank_mask:0xf
	s_waitcnt lgkmcnt(0)
	v_add_f32_e32 v16, v16, v17
	s_nop 1
	v_mov_b32_dpp v17, v16 quad_perm:[2,3,0,1] row_mask:0xf bank_mask:0xf
	s_waitcnt lgkmcnt(0)
	v_add_f32_e32 v16, v16, v17
	s_nop 1
	v_mov_b32_dpp v17, v16 row_half_mirror row_mask:0xf bank_mask:0xf
	s_waitcnt lgkmcnt(0)
	v_add_f32_e32 v16, v16, v17
	s_nop 1
	v_mov_b32_dpp v17, v16 row_mirror row_mask:0xf bank_mask:0xf
	s_waitcnt lgkmcnt(0)
	v_add_f32_e32 v16, v16, v17
	v_mov_b32_e32 v17, v16
	v_mov_b32_e32 v99, v16
	s_nop 1
	v_permlane16_swap_b32 v17, v99
	s_nop 1
	s_waitcnt lgkmcnt(0)
	v_add_f32_e32 v16, v17, v99
	v_mov_b32_e32 v17, v16
	v_mov_b32_e32 v100, v16
	s_nop 1
	v_permlane32_swap_b32 v17, v100
	s_nop 1
	s_waitcnt lgkmcnt(0)
	v_add_f32_e32 v16, v17, v100
	v_fmamk_f32 v16, v16, 0x3a800000, v94
	v_rsq_f32_e32 v24, v16
	s_nop 0
	v_pk_mul_f32 v[16:17], v[32:33], v[24:25] op_sel_hi:[1,0]
	v_pk_mul_f32 v[18:19], v[34:35], v[24:25] op_sel_hi:[1,0]
	v_pk_mul_f32 v[20:21], v[36:37], v[24:25] op_sel_hi:[1,0]
	v_pk_mul_f32 v[22:23], v[38:39], v[24:25] op_sel_hi:[1,0]
	v_pk_mul_f32 v[18:19], v[2:3], v[18:19]
	v_pk_mul_f32 v[16:17], v[0:1], v[16:17]
	v_pk_mul_f32 v[28:29], v[40:41], v[24:25] op_sel_hi:[1,0]
	v_pk_mul_f32 v[22:23], v[6:7], v[22:23]
	v_pk_mul_f32 v[20:21], v[4:5], v[20:21]
	global_store_dwordx4 v[26:27], v[16:19], off nt
	global_store_dwordx4 v[26:27], v[20:23], off offset:1024 nt
	s_nop 0
	v_pk_mul_f32 v[16:17], v[42:43], v[24:25] op_sel_hi:[1,0]
	s_nop 0
	v_pk_mul_f32 v[18:19], v[10:11], v[16:17]
	v_pk_mul_f32 v[16:17], v[8:9], v[28:29]
	global_store_dwordx4 v[26:27], v[16:19], off offset:2048 nt
	s_nop 1
	v_pk_mul_f32 v[16:17], v[44:45], v[24:25] op_sel_hi:[1,0]
	v_pk_mul_f32 v[18:19], v[46:47], v[24:25] op_sel_hi:[1,0]
	v_pk_mul_f32 v[16:17], v[12:13], v[16:17]
	v_pk_mul_f32 v[18:19], v[14:15], v[18:19]
	global_store_dwordx4 v[26:27], v[16:19], off offset:3072 nt

; template <int layer> __device__ __forceinline__ void layer_phases(const Ctx& c, unsigned char* lds) {
;     ...
;                     for (int r = 0; r < 2; ++r) { if (!live[r]) continue; const int m = mb_ + r * NGW; f32x4 v[4]; float s = 0.f;
; #pragma unroll
;                         for (int j = 0; j < 4; ++j) { const unsigned long long x = xw[r][j]; v[j] = (f32x4){bflo((unsigned)x), bfhi((unsigned)x), bflo((unsigned)(x >> 32)), bfhi((unsigned)(x >> 32))}; }
; #pragma unroll
;                         for (int sl = 0; sl < 2; ++sl) { const int p = pp[r][sl];
;                             if (p < tail0) {
; #pragma unroll
;                                 for (int j = 0; j < 4; ++j) { const unsigned long long a = yw[r][sl][j]; v[j] += (f32x4){bflo((unsigned)a), bfhi((unsigned)a), bflo((unsigned)(a >> 32)), bfhi((unsigned)(a >> 32))}; } }
;                             else { const f32x4* tp = (const f32x4*)((const float*)(ws + WS_YT) + (size_t)(p - tail0) * D) + lane;
; #pragma unroll
;                                 for (int kq = 0; kq < 4; ++kq)
; #pragma unroll
;                                     for (int j = 0; j < 4; ++j) v[j] += tp[(size_t)kq * 2048 * (D / 4) + 64 * j]; } }
; #pragma unroll
;                         for (int j = 0; j < 4; ++j) s += (v[j][0] * v[j][0] + v[j][1] * v[j][1]) + (v[j][2] * v[j][2] + v[j][3] * v[j][3]);
;                         const float rs = __builtin_amdgcn_rsqf(wave_sum(s) * (1.0f / D) + pg8::RMS_EPS);
;                         f32x4* xr = (f32x4*)(X + (size_t)m * D) + lane;
; #pragma unroll
;                         for (int j = 0; j < 4; ++j) __builtin_nontemporal_store(v[j] * rs * gfv[j], xr + 64 * j); }
.LBB0_1918:
	v_pk_mul_f32 v[16:17], v[34:35], v[34:35]
	v_pk_mul_f32 v[18:19], v[32:33], v[32:33]
	s_andn2_b64 vcc, exec, s[22:23]
	v_pk_mov_b32 v[20:21], v[18:19], v[16:17] op_sel:[1,0]
	v_mov_b32_e32 v19, v17
	v_pk_add_f32 v[16:17], v[20:21], v[18:19]
	v_pk_mul_f32 v[18:19], v[38:39], v[38:39]
	v_pk_add_f32 v[16:17], v[16:17], v[16:17] op_sel_hi:[0,1]
	v_pk_mul_f32 v[20:21], v[36:37], v[36:37]
	v_mul_f32_e32 v16, v40, v40
	v_pk_mov_b32 v[22:23], v[20:21], v[18:19] op_sel:[1,0]
	v_mov_b32_e32 v21, v19
	v_pk_add_f32 v[18:19], v[22:23], v[20:21]
	v_pk_fma_f32 v[20:21], v[40:41], v[40:41], v[16:17] op_sel_hi:[1,1,0]
	v_mul_f32_e32 v16, v42, v42
	v_pk_add_f32 v[18:19], v[18:19], v[18:19] op_sel_hi:[0,1]
	v_pk_fma_f32 v[22:23], v[42:43], v[42:43], v[16:17] op_sel_hi:[1,1,0]
	v_mul_f32_e32 v20, v44, v44
	v_mul_f32_e32 v22, v45, v45
	v_mul_f32_e32 v18, v46, v46
	v_mul_f32_e32 v16, v47, v47
	v_pk_add_f32 v[20:21], v[20:21], v[22:23]
	v_pk_add_f32 v[16:17], v[18:19], v[16:17]
	s_nop 0
	v_pk_add_f32 v[16:17], v[20:21], v[16:17]
	s_nop 0
	v_add_f32_e32 v16, v16, v17
	s_nop 1
	v_mov_b32_dpp v17, v16 quad_perm:[1,0,3,2] row_mask:0xf bank_mask:0xf
	s_waitcnt lgkmcnt(0)
	v_add_f32_e32 v16, v16, v17
	s_nop 1
	v_mov_b32_dpp v17, v16 quad_perm:[2,3,0,1] row_mask:0xf bank_mask:0xf
	s_waitcnt lgkmcnt(0)
	v_add_f32_e32 v16, v16, v17
	s_nop 1
	v_mov_b32_dpp v17, v16 row_half_mirror row_mask:0xf bank_mask:0xf
	s_waitcnt lgkmcnt(0)
	v_add_f32_e32 v16, v16, v17
	s_nop 1
	v_mov_b32_dpp v17, v16 row_mirror row_mask:0xf bank_mask:0xf
	s_waitcnt lgkmcnt(0)
	v_add_f32_e32 v16, v16, v17
	v_mov_b32_e32 v17, v16
	v_mov_b32_e32 v99, v16
	s_nop 1
	v_permlane16_swap_b32 v17, v99
	s_nop 1
	s_waitcnt lgkmcnt(0)
	v_add_f32_e32 v16, v17, v99
	v_mov_b32_e32 v17, v16
	v_mov_b32_e32 v100, v16
	s_nop 1
	v_permlane32_swap_b32 v17, v100
	s_nop 1
	s_waitcnt lgkmcnt(0)
	v_add_f32_e32 v16, v17, v100
	v_fmamk_f32 v16, v16, 0x3a800000, v94
	v_rsq_f32_e32 v28, v16
	s_nop 0
	v_pk_mul_f32 v[16:17], v[32:33], v[28:29] op_sel_hi:[1,0]
	v_pk_mul_f32 v[18:19], v[34:35], v[28:29] op_sel_hi:[1,0]
	v_pk_mul_f32 v[20:21], v[36:37], v[28:29] op_sel_hi:[1,0]
	v_pk_mul_f32 v[22:23], v[38:39], v[28:29] op_sel_hi:[1,0]
	v_pk_mul_f32 v[24:25], v[40:41], v[28:29] op_sel_hi:[1,0]
	v_pk_mul_f32 v[26:27], v[42:43], v[28:29] op_sel_hi:[1,0]
	v_pk_mul_f32 v[18:19], v[2:3], v[18:19]
	v_pk_mul_f32 v[16:17], v[0:1], v[16:17]
	v_pk_mul_f32 v[22:23], v[6:7], v[22:23]
	v_pk_mul_f32 v[20:21], v[4:5], v[20:21]
	v_pk_mul_f32 v[26:27], v[10:11], v[26:27]
	v_pk_mul_f32 v[24:25], v[8:9], v[24:25]
	global_store_dwordx4 v[58:59], v[16:19], off offset:-3072 nt
	global_store_dwordx4 v[58:59], v[20:23], off offset:-2048 nt
	global_store_dwordx4 v[58:59], v[24:27], off offset:-1024 nt
	v_pk_mul_f32 v[16:17], v[44:45], v[28:29] op_sel_hi:[1,0]
	v_pk_mul_f32 v[18:19], v[46:47], v[28:29] op_sel_hi:[1,0]
	v_pk_mul_f32 v[16:17], v[12:13], v[16:17]
	v_pk_mul_f32 v[18:19], v[14:15], v[18:19]
	global_store_dwordx4 v[58:59], v[16:19], off nt
	s_cbranch_vccnz .LBB0_1909
	s_waitcnt vmcnt(15)
	v_lshlrev_b32_e32 v44, 16, v84
	v_and_b32_e32 v45, 0xffff0000, v84
	v_lshlrev_b32_e32 v46, 16, v85
	v_and_b32_e32 v47, 0xffff0000, v85
	s_waitcnt vmcnt(14)
	v_lshlrev_b32_e32 v40, 16, v82
	v_and_b32_e32 v41, 0xffff0000, v82
	v_lshlrev_b32_e32 v42, 16, v83
	v_and_b32_e32 v43, 0xffff0000, v83
	s_waitcnt vmcnt(13)
	v_lshlrev_b32_e32 v36, 16, v80
	v_and_b32_e32 v37, 0xffff0000, v80
	v_lshlrev_b32_e32 v38, 16, v81
	v_and_b32_e32 v39, 0xffff0000, v81
	s_waitcnt vmcnt(12)
	v_lshlrev_b32_e32 v32, 16, v78
	v_and_b32_e32 v33, 0xffff0000, v78
	v_lshlrev_b32_e32 v34, 16, v79
	v_and_b32_e32 v35, 0xffff0000, v79
	s_andn2_b64 vcc, exec, s[20:21]
	s_mov_b64 s[20:21], -1
	s_cbranch_vccnz .LBB0_1921
	s_sub_i32 s2, s16, s30
	s_lshl_b64 s[20:21], s[2:3], 12
	v_lshl_add_u64 v[118:119], v[56:57], 0, s[20:21]
	v_add_co_u32_e32 v102, vcc, s34, v118
	global_load_dwordx4 v[16:19], v[118:119], off
	global_load_dwordx4 v[20:23], v[118:119], off offset:1024
	global_load_dwordx4 v[24:27], v[118:119], off offset:2048
	global_load_dwordx4 v[28:31], v[118:119], off offset:3072
	v_addc_co_u32_e32 v103, vcc, 0, v119, vcc
	v_add_co_u32_e32 v120, vcc, s35, v118
	global_load_dwordx4 v[78:81], v[102:103], off
	global_load_dwordx4 v[82:85], v[102:103], off offset:1024
	global_load_dwordx4 v[86:89], v[102:103], off offset:2048
	global_load_dwordx4 v[90:93], v[102:103], off offset:3072
	v_addc_co_u32_e32 v121, vcc, 0, v119, vcc
	v_add_co_u32_e32 v130, vcc, s36, v118
	global_load_dwordx4 v[102:105], v[120:121], off
	global_load_dwordx4 v[106:109], v[120:121], off offset:1024
	global_load_dwordx4 v[110:113], v[120:121], off offset:2048
	global_load_dwordx4 v[114:117], v[120:121], off offset:3072
	v_addc_co_u32_e32 v131, vcc, 0, v119, vcc
	global_load_dwordx4 v[118:121], v[130:131], off
	global_load_dwordx4 v[122:125], v[130:131], off offset:1024
	global_load_dwordx4 v[126:129], v[130:131], off offset:2048
	s_nop 0
	global_load_dwordx4 v[130:133], v[130:131], off offset:3072
	s_waitcnt vmcnt(15)
	v_pk_add_f32 v[18:19], v[18:19], v[46:47]
	v_pk_add_f32 v[16:17], v[16:17], v[44:45]
	s_waitcnt vmcnt(14)
	v_pk_add_f32 v[22:23], v[22:23], v[42:43]
	v_pk_add_f32 v[20:21], v[20:21], v[40:41]
	s_waitcnt vmcnt(13)
	v_pk_add_f32 v[26:27], v[26:27], v[38:39]
	v_pk_add_f32 v[24:25], v[24:25], v[36:37]
	s_waitcnt vmcnt(12)
	v_pk_add_f32 v[30:31], v[30:31], v[34:35]
	v_pk_add_f32 v[28:29], v[28:29], v[32:33]
	s_waitcnt vmcnt(11)
	v_pk_add_f32 v[18:19], v[18:19], v[80:81]
	v_pk_add_f32 v[16:17], v[16:17], v[78:79]
	s_waitcnt vmcnt(10)
	v_pk_add_f32 v[22:23], v[22:23], v[84:85]
	v_pk_add_f32 v[20:21], v[20:21], v[82:83]
	s_waitcnt vmcnt(9)
	v_pk_add_f32 v[26:27], v[26:27], v[88:89]
	v_pk_add_f32 v[24:25], v[24:25], v[86:87]
	s_waitcnt vmcnt(8)
	v_pk_add_f32 v[30:31], v[30:31], v[92:93]
	v_pk_add_f32 v[28:29], v[28:29], v[90:91]
	s_waitcnt vmcnt(7)
	v_pk_add_f32 v[18:19], v[18:19], v[104:105]
	v_pk_add_f32 v[16:17], v[16:17], v[102:103]
	s_waitcnt vmcnt(6)
	v_pk_add_f32 v[22:23], v[22:23], v[108:109]
	v_pk_add_f32 v[20:21], v[20:21], v[106:107]
	s_waitcnt vmcnt(5)
	v_pk_add_f32 v[26:27], v[26:27], v[112:113]
	v_pk_add_f32 v[24:25], v[24:25], v[110:111]
	s_waitcnt vmcnt(4)
	v_pk_add_f32 v[30:31], v[30:31], v[116:117]
	v_pk_add_f32 v[28:29], v[28:29], v[114:115]
	s_waitcnt vmcnt(3)
	v_pk_add_f32 v[18:19], v[18:19], v[120:121]
	v_pk_add_f32 v[16:17], v[16:17], v[118:119]
	s_waitcnt vmcnt(2)
	v_pk_add_f32 v[22:23], v[22:23], v[124:125]
	v_pk_add_f32 v[20:21], v[20:21], v[122:123]
	s_waitcnt vmcnt(1)
	v_pk_add_f32 v[26:27], v[26:27], v[128:129]
	v_pk_add_f32 v[24:25], v[24:25], v[126:127]
	s_waitcnt vmcnt(0)
	v_pk_add_f32 v[30:31], v[30:31], v[132:133]
	v_pk_add_f32 v[28:29], v[28:29], v[130:131]
	s_cbranch_execnz .LBB0_1923
	s_branch .LBB0_1922
